# in-proj GEMM main loop rewritten by hand (LDS double buffer, 1 barrier per k-tile, interleaved LDS/VMEM ops, conflict-free layouts) + role-1 WG starts in-proj phase 1792 cycles late
# speedup vs baseline: 1.0147x; 1.0147x over previous
; #define PR_BEGIN(id) do { if (PROBE_SP == (id)) c.prt = __builtin_amdgcn_s_memrealtime(); } while (0)
; #define PR_END(id) do { if (PROBE_SP == (id)) c.pracc += __builtin_amdgcn_s_memrealtime() - c.prt; } while (0)
; __global__ void __launch_bounds__(NTHR, 2) mk_fwd(Params prm) {
;     ...
;     for (int ph = prm.ph_lo; ph < prm.ph_hi; ++ph) {
;         if (PROBE_SP >= 0) pr_t0 = __builtin_amdgcn_s_memrealtime();
;         asm volatile("" : "+s"(c.p));
;         { int t_ = threadIdx.x; asm volatile("" : "+v"(t_)); c.tid = t_; }
;         if (ph == 0) {
;             const bool split = G >= 384;
;             const int g2 = split ? (bid >= 256 ? gtid - 65536 : 0x3fffffff) : gtid, gth2 = split ? gthreads - 65536 : gthreads;
;             ph_prep(c, g2, gth2, bid, G, (float*)smem_raw); PR_BEGIN(124); cvt_small(c, g2, gth2); PR_END(124); }
;         else if (ph == 1) ph_norm1(c, 0, gw, nwaves, smem_raw);
;         else {
;             const int layer = (ph - 2) / PH_PER_LAYER, sp = (ph - 2) % PH_PER_LAYER;
;             switch (sp) {
;             case 0: for (int t = bid; t < 136 * 18 + (layer == 0 ? 5120 : 0); t += G) { asm volatile("" : "+v"(c.tid)); if (t < 136 * 18) ph_inproj_mfma(c, layer, t, smem_raw); else ph_prepB(c, t - 136 * 18); } break;
.LBB0_13:
	s_lshr_b32 s6, 0x804, s66
	s_bitcmp1_b32 s6, 0
	s_cbranch_scc0 .Lstag_done
	ds_read_b32 v2, v146
	s_waitcnt lgkmcnt(0)
	v_readfirstlane_b32 s6, v2
	s_cmp_eq_u32 s6, 0
	s_cbranch_scc1 .Lstag_done
	s_sleep 28

;     template <class T> __device__ __forceinline__ T* w(size_t off) const { return (T*)(p->ws + off); }
;     const int lane = tid & 63, wid = tid >> 6, wr = wid >> 1, wc = wid & 1, fr = lane & 15, fq = lane >> 4;
; #pragma unroll
;     for (int m = 0; m < 4; ++m)
; #pragma unroll
;         for (int n = 0; n < 4; ++n) acc[m][n] = (f32x4){0.f, 0.f, 0.f, 0.f};
;     unsigned ao[4];
; #pragma unroll
;     for (int i = 0; i < 4; ++i) ao[i] = arow((tid >> 3) + 32 * i) + (tid & 7) * 8;
;     const int bk = tid >> 4, bnc = tid & 15;
;     constexpr int NRB = B_F32 ? 8 : 4;
;     u32x4 ra0[4], ra1[4]; u32x4 rb0[NRB], rb1[NRB];
;     auto gloadA = [&](int kt, u32x4 (&ra)[4]) __attribute__((always_inline)) {
; #pragma unroll
;         for (int i = 0; i < 4; ++i) ra[i] = *(const u32x4*)(Abase + (ao[i] + kt * 64));
;     };
;     auto gloadB = [&](int kt, u32x4 (&rb)[NRB]) __attribute__((always_inline)) {
;         if (B_F32) {
;             const float* bp = (const float*)Bbase + (boff + (unsigned)((kt * 64 + bk) * ldb));
; #pragma unroll
;             for (int i = 0; i < 4; ++i) {
;                 if (bval) { rb[2 * i] = *(const u32x4*)(bp + (unsigned)(16 * i * ldb)); rb[2 * i + 1] = *(const u32x4*)(bp + (unsigned)(16 * i * ldb) + 4); }
;                 else { rb[2 * i] = (u32x4){0u, 0u, 0u, 0u}; rb[2 * i + 1] = rb[2 * i]; }
;             }
;         } else {
;             const bf16* bp = (const bf16*)Bbase + (boff + (unsigned)((kt * 64 + bk) * ldb));
; #pragma unroll
;             for (int i = 0; i < 4; ++i) rb[i] = bval ? *(const u32x4*)(bp + (unsigned)(16 * i * ldb)) : (u32x4){0u, 0u, 0u, 0u};
;         }
;     };
; __device__ __forceinline__ void ph_inproj_mfma(const Ctx& c, int layer, int tile, unsigned char* lds) {
;     const int mt = tile / 18, nt = tile % 18;
;     const bf16* HA = c.w<bf16>(WS_HA) + (size_t)mt * 128 * D;
;     f32x4 acc[4][4];
;     const int vc = nt * 128 + (c.tid & 15) * 8;
;     gemm_tile<false, 1>(c.tid, lds, HA, [&](int r) __attribute__((always_inline)) { return (unsigned)(r * D); }, c.w<bf16>(WS_BIN) + (size_t)layer * D * DINV, (unsigned)vc, DINV, true, D, acc);
.LBB0_544:
	s_andn2_b64 vcc, exec, s[0:1]
	s_cbranch_vccnz .LBB0_533
	s_mul_hi_i32 s0, s60, 0x38e38e39
	s_load_dwordx2 s[42:43], s[4:5], 0x130
	s_lshr_b32 s1, s0, 31
	s_ashr_i32 s0, s0, 2
	s_add_i32 s28, s0, s1
	s_mul_i32 s0, s28, 18
	s_ashr_i32 s29, s28, 31
	s_sub_i32 s17, s60, s0
	s_lshl_b64 s[0:1], s[28:29], 18
	s_waitcnt lgkmcnt(0)
	s_add_u32 s0, s42, s0
	s_addc_u32 s1, s43, s1
	s_add_u32 s44, s0, 0x45c6000
	s_addc_u32 s45, s1, 0
	s_lshl_b32 s61, s17, 7
	s_add_u32 s0, s42, s59
	s_waitcnt vmcnt(0)
	v_lshlrev_b32_e32 v12, 3, v147
	s_addc_u32 s1, s43, s58
	s_add_u32 s46, s0, 0x18095100
	v_lshlrev_b32_e32 v2, 7, v147
	v_and_b32_e32 v4, 56, v12
	s_movk_i32 s0, 0xfc00
	v_and_b32_e32 v155, 15, v147
	v_and_or_b32 v2, v2, s0, v4
	v_lshrrev_b32_e32 v5, 1, v147
	s_mov_b32 s0, 0x3ffffc0
	v_bfe_u32 v157, v147, 4, 2
	v_and_or_b32 v5, v5, s0, v155
	v_bfe_u32 v7, v147, 4, 1
	v_lshlrev_b32_e32 v16, 6, v5
	v_lshlrev_b32_e32 v118, 3, v157
	v_bfe_u32 v5, v147, 2, 2
	v_lshlrev_b32_e32 v9, 2, v7
	v_or3_b32 v5, v9, v5, v118
	v_lshlrev_b32_e32 v9, 1, v147
	v_and_b32_e32 v9, 0x80, v9
	s_movk_i32 s7, 0x120
	v_mad_u32_u24 v5, v5, s7, v9
	v_and_b32_e32 v13, 0x78, v12
	v_add_u32_e32 v4, 0x8000, v2
	v_add_u32_e32 v6, 0x10000, v2
	v_ashrrev_i32_e32 v15, 4, v147
	v_and_or_b32 v119, v12, 24, v5
	v_cmp_eq_u32_e32 vcc, 0, v7
	v_mov_b32_e32 v5, v3
	v_mov_b32_e32 v7, v3
	s_movk_i32 s0, 0x900
	v_or_b32_e32 v14, s61, v13
	v_lshl_add_u64 v[4:5], v[4:5], 1, s[44:45]
	v_lshl_add_u64 v[6:7], v[6:7], 1, s[44:45]
	v_mul_lo_u32 v18, v15, s0
	s_addc_u32 s47, s1, 0
	v_add_u32_e32 v8, 0x18000, v2
	v_mov_b32_e32 v9, v3
	v_add_u32_e32 v6, v14, v18
	v_mov_b32_e32 v7, v3
	v_lshl_add_u64 v[4:5], v[8:9], 1, s[44:45]
	v_lshl_add_u64 v[6:7], v[6:7], 1, s[46:47]
	s_mov_b32 s0, 0x12000
	v_cndmask_b32_e32 v17, v236, v237, vcc
	v_add_co_u32_e32 v4, vcc, s0, v6
	s_mov_b32 s0, 0x24000
	s_nop 0
	v_addc_co_u32_e32 v5, vcc, 0, v7, vcc
	v_add_co_u32_e32 v8, vcc, s0, v6
	s_mov_b32 s0, 0x36000
	s_nop 0
	v_addc_co_u32_e32 v9, vcc, 0, v7, vcc
	v_add_co_u32_e32 v4, vcc, s0, v6
	v_lshl_add_u64 v[10:11], v[2:3], 1, s[44:45]
	s_nop 0
	v_addc_co_u32_e32 v5, vcc, 0, v7, vcc
	v_add_u32_e32 v6, 0x8040, v2
	v_mov_b32_e32 v7, v3
	v_lshl_add_u64 v[6:7], v[6:7], 1, s[44:45]
	v_add_u32_e32 v4, 0x10040, v2
	v_mov_b32_e32 v5, v3
	v_lshl_add_u64 v[4:5], v[4:5], 1, s[44:45]
	v_add_u32_e32 v6, 0x18040, v2
	v_mov_b32_e32 v7, v3
	v_lshl_add_u64 v[6:7], v[6:7], 1, s[44:45]
	v_and_b32_e32 v4, 1, v147
	v_cmp_eq_u32_e64 s[0:1], 0, v4
	v_bfe_i32 v4, v147, 2, 1
	v_and_b32_e32 v4, 0x2040, v4
	v_and_b32_e32 v5, 0xffffffc0, v12
	v_lshl_add_u32 v7, s60, 7, v18
	v_add_u32_e32 v4, v4, v5
	v_lshlrev_b32_e32 v5, 4, v147
	v_mul_lo_u32 v6, v15, s7
	v_or_b32_e32 v7, v7, v13
	s_mul_i32 s7, s28, 0x900
	v_lshlrev_b32_e32 v122, 4, v157
	v_and_b32_e32 v5, 48, v5
	v_lshlrev_b32_e32 v153, 4, v155
	v_subrev_u32_e32 v7, s7, v7
	v_mov_b32_e32 v20, 0
	v_lshrrev_b32_e32 v149, 4, v147
	s_mov_b32 s6, 0
	v_add_u32_e32 v116, 0x48000, v7
	v_add_u32_e32 v120, 0x10080, v2
	v_add_u32_e32 v123, v4, v5
	v_add_u32_e32 v124, v6, v153
	v_add_u32_e32 v125, v16, v122
	v_add_u32_e32 v126, v119, v17
	v_lshlrev_b32_e32 v206, 1, v2
	v_add_u32_e32 v207, 0x10000, v206
	v_add_u32_e32 v208, 0x20000, v206
	v_add_u32_e32 v209, 0x30000, v206
	v_lshlrev_b32_e32 v210, 1, v116
	v_add_u32_e32 v210, 0xfff70000, v210
	v_add_u32_e32 v211, 0x12000, v210
	v_add_u32_e32 v212, 0x24000, v210
	v_add_u32_e32 v213, 0x36000, v210
	v_bfe_u32 v215, v147, 5, 2
	v_sub_u32_e32 v215, 0, v215
	v_and_b32_e32 v215, 3, v215
	v_lshlrev_b32_e32 v215, 4, v215
	v_xor_b32_e32 v215, v123, v215
	v_bfe_u32 v216, v147, 2, 2
	v_sub_u32_e32 v216, 0, v216
	v_and_b32_e32 v216, 3, v216
	v_lshlrev_b32_e32 v216, 4, v216
	v_xor_b32_e32 v216, v125, v216
	v_and_b32_e32 v217, 15, v147
	v_lshlrev_b32_e32 v217, 4, v217
	v_bfe_u32 v120, v147, 7, 1
	v_lshlrev_b32_e32 v120, 7, v120
	v_xor_b32_e32 v217, v217, v120
	v_lshrrev_b32_e32 v120, 4, v147
	v_mul_u32_u24_e32 v120, 0x120, v120
	v_add_u32_e32 v217, v217, v120
	v_add_u32_e32 v214, 0x9000, v217
	v_bfe_u32 v218, v147, 4, 2
	v_lshlrev_b32_e32 v218, 3, v218
	v_bfe_u32 v120, v147, 2, 2
	v_add_u32_e32 v218, v218, v120
	v_mul_u32_u24_e32 v218, 0x120, v218
	v_lshrrev_b32_e32 v120, 6, v147
	v_lshrrev_b32_e32 v121, 4, v147
	v_xor_b32_e32 v120, v120, v121
	v_and_b32_e32 v120, 1, v120
	v_lshlrev_b32_e32 v120, 7, v120
	v_and_b32_e32 v121, 3, v147
	v_lshlrev_b32_e32 v121, 3, v121
	v_or3_b32 v218, v218, v120, v121
	global_load_dwordx4 v[80:83], v206, s[44:45]
	global_load_dwordx4 v[68:71], v207, s[44:45]
	global_load_dwordx4 v[72:75], v208, s[44:45]
	global_load_dwordx4 v[76:79], v209, s[44:45]
	global_load_dwordx4 v[88:91], v210, s[46:47]
	global_load_dwordx4 v[96:99], v211, s[46:47]
	global_load_dwordx4 v[108:111], v212, s[46:47]
	global_load_dwordx4 v[112:115], v213, s[46:47]
	s_add_u32 s46, s46, 0x48000
	s_addc_u32 s47, s47, 0
	global_load_dwordx4 v[84:87], v206, s[44:45] offset:128
	global_load_dwordx4 v[92:95], v207, s[44:45] offset:128
	global_load_dwordx4 v[100:103], v208, s[44:45] offset:128
	global_load_dwordx4 v[104:107], v209, s[44:45] offset:128
	global_load_dwordx4 v[190:193], v210, s[46:47]
	global_load_dwordx4 v[194:197], v211, s[46:47]
	global_load_dwordx4 v[198:201], v212, s[46:47]
	global_load_dwordx4 v[202:205], v213, s[46:47]
	s_add_u32 s46, s46, 0x48000
	s_addc_u32 s47, s47, 0
	v_mov_b32_e32 v21, v20
	v_mov_b32_e32 v22, v20
	v_mov_b32_e32 v23, v20
	v_mov_b32_e32 v32, v20
	v_mov_b32_e32 v33, v20
	v_mov_b32_e32 v34, v20
	v_mov_b32_e32 v35, v20
	v_mov_b32_e32 v4, v20
	v_mov_b32_e32 v5, v20
	v_mov_b32_e32 v6, v20
	v_mov_b32_e32 v7, v20
	v_mov_b32_e32 v8, v20
	v_mov_b32_e32 v9, v20
	v_mov_b32_e32 v10, v20
	v_mov_b32_e32 v11, v20
	v_mov_b32_e32 v12, v20
	v_mov_b32_e32 v13, v20
	v_mov_b32_e32 v14, v20
	v_mov_b32_e32 v15, v20
	v_mov_b32_e32 v16, v20
	v_mov_b32_e32 v17, v20
	v_mov_b32_e32 v18, v20
	v_mov_b32_e32 v19, v20
	v_mov_b32_e32 v24, v20
	v_mov_b32_e32 v25, v20
	v_mov_b32_e32 v26, v20
	v_mov_b32_e32 v27, v20
	v_mov_b32_e32 v28, v20
	v_mov_b32_e32 v29, v20
	v_mov_b32_e32 v30, v20
	v_mov_b32_e32 v31, v20
	v_mov_b32_e32 v36, v20
	v_mov_b32_e32 v37, v20
	v_mov_b32_e32 v38, v20
	v_mov_b32_e32 v39, v20
	v_mov_b32_e32 v40, v20
	v_mov_b32_e32 v41, v20
	v_mov_b32_e32 v42, v20
	v_mov_b32_e32 v43, v20
	v_mov_b32_e32 v44, v20
	v_mov_b32_e32 v45, v20
	v_mov_b32_e32 v46, v20
	v_mov_b32_e32 v47, v20
	v_mov_b32_e32 v48, v20
	v_mov_b32_e32 v49, v20
	v_mov_b32_e32 v50, v20
	v_mov_b32_e32 v51, v20
	v_mov_b32_e32 v52, v20
	v_mov_b32_e32 v53, v20
	v_mov_b32_e32 v54, v20
	v_mov_b32_e32 v55, v20
	v_mov_b32_e32 v56, v20
	v_mov_b32_e32 v57, v20
	v_mov_b32_e32 v58, v20
	v_mov_b32_e32 v59, v20
	v_mov_b32_e32 v60, v20
	v_mov_b32_e32 v61, v20
	v_mov_b32_e32 v62, v20
	v_mov_b32_e32 v63, v20
	v_mov_b32_e32 v64, v20
	v_mov_b32_e32 v65, v20
	v_mov_b32_e32 v66, v20
	v_mov_b32_e32 v67, v20
	s_waitcnt vmcnt(8)
	s_barrier
;     ...
;     auto lstore = [&](const u32x4 (&ra)[4], const u32x4 (&rb)[NRB]) __attribute__((always_inline)) {
; #pragma unroll
;         for (int i = 0; i < 4; ++i) { const int row = (tid >> 3) + 32 * i, kc = tid & 7;
;             const u32x4 v = (kc & 1) ? (u32x4){ra[i][2], ra[i][3], ra[i][0], ra[i][1]} : ra[i];
;             *(u32x4*)(lds + (kc >> 2) * GA_KH + row * 64 + (kc & 3) * 16) = v; }
; #pragma unroll
;         for (int i = 0; i < 4; ++i) { const int k = bk + 16 * i;
;             u32x4 v;
;             if (B_F32) { const f32x4 x = __builtin_bit_cast(f32x4, rb[2 * i]), y = __builtin_bit_cast(f32x4, rb[2 * i + 1]);
;                 v[0] = pk2bf(x[0], x[1]); v[1] = pk2bf(x[2], x[3]); v[2] = pk2bf(y[0], y[1]); v[3] = pk2bf(y[2], y[3]); }
;             else v = rb[i];
;             *(u32x4*)(lds + GB_OFF + k * GB_ST + bnc * 16) = v; }
;     };
;     const lds_cptr la = (lds_cptr)lds + (wr * 64 + fr) * 64 + fq * 16;
;     const lds_cptr lb = (lds_cptr)lds + GB_OFF + (8 * fq + (fr >> 2) + (fq & 1) * 4) * GB_ST + wc * 128 + (fr & 3) * 8;
;     const int bsw = (fq & 1) ? -4 * GB_ST : 4 * GB_ST;
;     auto compute = [&]() __attribute__((always_inline)) {
; #pragma unroll
;         for (int kh = 0; kh < 2; ++kh) {
;             bf16x8 af[4], bfr[4];
; #pragma unroll
;             for (int m = 0; m < 4; ++m) af[m] = *(const LAS bf16x8*)(la + kh * GA_KH + m * 1024);
; #pragma unroll
;             for (int n = 0; n < 4; ++n) {
;                 const s16x4 r0 = lds_tr(lb + kh * 32 * GB_ST + n * 32), r1 = lds_tr(lb + kh * 32 * GB_ST + n * 32 + bsw);
;                 bfr[n] = (bf16x8){r0[0], r0[1], r0[2], r0[3], r1[0], r1[1], r1[2], r1[3]};
;             }
; #pragma unroll
;             for (int m = 0; m < 4; ++m)
; #pragma unroll
;                 for (int n = 0; n < 4; ++n) acc[m][n] = __builtin_amdgcn_mfma_f32_16x16x32_bf16(bfr[n], af[m], acc[m][n], 0, 0, 0);
;         }
;     };
;     ...
;     if (DEEP == 1) {
;         gloadA(0, ra0); gloadB(0, rb0); gloadA(1, ra1);
;         for (int kt = 0; kt < nk; kt += 2) {
;             __syncthreads();
;             lstore(ra0, rb0);
;             __syncthreads();
;             gloadB(kt + 1, rb0);
;             if (kt + 2 < nk) gloadA(kt + 2, ra0);
;             compute();
;             __syncthreads();
;             lstore(ra1, rb0);
;             __syncthreads();
;             if (kt + 2 < nk) gloadB(kt + 2, rb0);
	ds_write_b128 v215, v[80:83]
	ds_write_b128 v215, v[68:71] offset:2048
	ds_write_b128 v215, v[72:75] offset:4096
	ds_write_b128 v215, v[76:79] offset:6144
	ds_write_b128 v217, v[88:91] offset:16512
	ds_write_b128 v217, v[96:99] offset:21120
	ds_write_b128 v217, v[108:111] offset:25728
	ds_write_b128 v217, v[112:115] offset:30336
	global_load_dwordx4 v[80:83], v206, s[44:45] offset:256
	global_load_dwordx4 v[68:71], v207, s[44:45] offset:256
	global_load_dwordx4 v[72:75], v208, s[44:45] offset:256
	global_load_dwordx4 v[76:79], v209, s[44:45] offset:256
	global_load_dwordx4 v[88:91], v210, s[46:47]
	global_load_dwordx4 v[96:99], v211, s[46:47]
	global_load_dwordx4 v[108:111], v212, s[46:47]
	global_load_dwordx4 v[112:115], v213, s[46:47]
	s_add_u32 s46, s46, 0x48000
	s_addc_u32 s47, s47, 0
	s_add_u32 s100, s46, 0x48000
	s_addc_u32 s101, s47, 0
	s_waitcnt lgkmcnt(0)
	s_barrier
.Lip_loop:
	ds_read_b64_tr_b16 v[158:159], v218 offset:16512
	ds_read_b64_tr_b16 v[160:161], v218 offset:17664
	ds_read_b128 v[128:131], v216
	ds_read_b64_tr_b16 v[162:163], v218 offset:16544
	ds_read_b64_tr_b16 v[164:165], v218 offset:17696
	s_waitcnt lgkmcnt(2)
	v_mfma_f32_16x16x32_bf16 v[64:67], v[158:161], v[128:131], v[64:67]
	ds_read_b64_tr_b16 v[166:167], v218 offset:16576
	ds_read_b64_tr_b16 v[168:169], v218 offset:17728
	s_waitcnt lgkmcnt(2)
	v_mfma_f32_16x16x32_bf16 v[60:63], v[162:165], v[128:131], v[60:63]
	ds_read_b64_tr_b16 v[170:171], v218 offset:16608
	ds_read_b64_tr_b16 v[172:173], v218 offset:17760
	s_waitcnt lgkmcnt(2)
	v_mfma_f32_16x16x32_bf16 v[56:59], v[166:169], v[128:131], v[56:59]
	ds_read_b128 v[132:135], v216 offset:1024
	s_waitcnt lgkmcnt(1)
	v_mfma_f32_16x16x32_bf16 v[52:55], v[170:173], v[128:131], v[52:55]
	ds_read_b128 v[136:139], v216 offset:2048
	s_waitcnt lgkmcnt(1)
	v_mfma_f32_16x16x32_bf16 v[48:51], v[158:161], v[132:135], v[48:51]
	ds_read_b128 v[140:143], v216 offset:3072
	v_mfma_f32_16x16x32_bf16 v[44:47], v[162:165], v[132:135], v[44:47]
	ds_read_b64_tr_b16 v[174:175], v218 offset:25728
	ds_read_b64_tr_b16 v[176:177], v218 offset:26880
	v_mfma_f32_16x16x32_bf16 v[40:43], v[166:169], v[132:135], v[40:43]
	ds_read_b64_tr_b16 v[178:179], v218 offset:25760
	ds_read_b64_tr_b16 v[180:181], v218 offset:26912
	v_mfma_f32_16x16x32_bf16 v[36:39], v[170:173], v[132:135], v[36:39]
	ds_read_b128 v[128:131], v216 offset:8256
	s_waitcnt lgkmcnt(6)
	v_mfma_f32_16x16x32_bf16 v[28:31], v[158:161], v[136:139], v[28:31]
	ds_read_b64_tr_b16 v[182:183], v218 offset:25792
	ds_read_b64_tr_b16 v[184:185], v218 offset:26944
	v_mfma_f32_16x16x32_bf16 v[24:27], v[162:165], v[136:139], v[24:27]
	ds_read_b64_tr_b16 v[186:187], v218 offset:25824
	ds_read_b64_tr_b16 v[188:189], v218 offset:26976
	v_mfma_f32_16x16x32_bf16 v[16:19], v[166:169], v[136:139], v[16:19]
	s_waitcnt vmcnt(8)
	ds_write_b128 v215, v[84:87] offset:36864
	v_mfma_f32_16x16x32_bf16 v[12:15], v[170:173], v[136:139], v[12:15]
	ds_read_b128 v[132:135], v216 offset:9280
	s_waitcnt lgkmcnt(11)
	v_mfma_f32_16x16x32_bf16 v[8:11], v[158:161], v[140:143], v[8:11]
	ds_write_b128 v215, v[92:95] offset:38912
	v_mfma_f32_16x16x32_bf16 v[4:7], v[162:165], v[140:143], v[4:7]
	ds_write_b128 v215, v[100:103] offset:40960
	v_mfma_f32_16x16x32_bf16 v[32:35], v[166:169], v[140:143], v[32:35]
	ds_write_b128 v215, v[104:107] offset:43008
	v_mfma_f32_16x16x32_bf16 v[20:23], v[170:173], v[140:143], v[20:23]
	ds_read_b128 v[136:139], v216 offset:10304
	s_waitcnt lgkmcnt(10)
	v_mfma_f32_16x16x32_bf16 v[64:67], v[174:177], v[128:131], v[64:67]
	ds_write_b128 v214, v[190:193] offset:16512
	v_mfma_f32_16x16x32_bf16 v[60:63], v[178:181], v[128:131], v[60:63]
	ds_write_b128 v214, v[194:197] offset:21120
	s_waitcnt lgkmcnt(10)
	v_mfma_f32_16x16x32_bf16 v[56:59], v[182:185], v[128:131], v[56:59]
	ds_write_b128 v214, v[198:201] offset:25728
	s_waitcnt lgkmcnt(9)
	v_mfma_f32_16x16x32_bf16 v[52:55], v[186:189], v[128:131], v[52:55]
	ds_read_b128 v[140:143], v216 offset:11328
	s_waitcnt lgkmcnt(8)
	v_mfma_f32_16x16x32_bf16 v[48:51], v[174:177], v[132:135], v[48:51]
	ds_write_b128 v214, v[202:205] offset:30336
	v_mfma_f32_16x16x32_bf16 v[44:47], v[178:181], v[132:135], v[44:47]
	global_load_dwordx4 v[84:87], v206, s[44:45] offset:384
	v_mfma_f32_16x16x32_bf16 v[40:43], v[182:185], v[132:135], v[40:43]
	global_load_dwordx4 v[92:95], v207, s[44:45] offset:384
	v_mfma_f32_16x16x32_bf16 v[36:39], v[186:189], v[132:135], v[36:39]
	global_load_dwordx4 v[100:103], v208, s[44:45] offset:384
	s_waitcnt lgkmcnt(5)
	v_mfma_f32_16x16x32_bf16 v[28:31], v[174:177], v[136:139], v[28:31]
	global_load_dwordx4 v[104:107], v209, s[44:45] offset:384
	v_mfma_f32_16x16x32_bf16 v[24:27], v[178:181], v[136:139], v[24:27]
	global_load_dwordx4 v[190:193], v210, s[46:47]
	v_mfma_f32_16x16x32_bf16 v[16:19], v[182:185], v[136:139], v[16:19]
	global_load_dwordx4 v[194:197], v211, s[46:47]
	v_mfma_f32_16x16x32_bf16 v[12:15], v[186:189], v[136:139], v[12:15]
	global_load_dwordx4 v[198:201], v212, s[46:47]
	s_waitcnt lgkmcnt(1)
	v_mfma_f32_16x16x32_bf16 v[8:11], v[174:177], v[140:143], v[8:11]
	global_load_dwordx4 v[202:205], v213, s[46:47]
	v_mfma_f32_16x16x32_bf16 v[4:7], v[178:181], v[140:143], v[4:7]
	v_mfma_f32_16x16x32_bf16 v[32:35], v[182:185], v[140:143], v[32:35]
	v_mfma_f32_16x16x32_bf16 v[20:23], v[186:189], v[140:143], v[20:23]
	s_waitcnt lgkmcnt(0)
	s_barrier
	s_cmp_lt_u32 s6, 12
	s_cbranch_scc0 .Lip_h1_last
; #define LAS __attribute__((address_space(3)))
; __device__ __forceinline__ s16x4 lds_tr(lds_cptr p) { return __builtin_bit_cast(s16x4, __builtin_amdgcn_ds_read_tr16_b64_v4i16((LAS s16x4*)p)); }
;     ...
;     auto compute = [&]() __attribute__((always_inline)) {
; #pragma unroll
;         for (int kh = 0; kh < 2; ++kh) {
;             bf16x8 af[4], bfr[4];
; #pragma unroll
;             for (int m = 0; m < 4; ++m) af[m] = *(const LAS bf16x8*)(la + kh * GA_KH + m * 1024);
; #pragma unroll
;             for (int n = 0; n < 4; ++n) {
;                 const s16x4 r0 = lds_tr(lb + kh * 32 * GB_ST + n * 32), r1 = lds_tr(lb + kh * 32 * GB_ST + n * 32 + bsw);
;                 bfr[n] = (bf16x8){r0[0], r0[1], r0[2], r0[3], r1[0], r1[1], r1[2], r1[3]};
;             }
; #pragma unroll
;             for (int m = 0; m < 4; ++m)
; #pragma unroll
;                 for (int n = 0; n < 4; ++n) acc[m][n] = __builtin_amdgcn_mfma_f32_16x16x32_bf16(bfr[n], af[m], acc[m][n], 0, 0, 0);
;         }
;     };
;     ...
;             __syncthreads();
;             lstore(ra1, rb0);
;             __syncthreads();
;             if (kt + 2 < nk) gloadB(kt + 2, rb0);
;             if (kt + 3 < nk) gloadA(kt + 3, ra1);
;             compute();
;         }
	ds_read_b64_tr_b16 v[158:159], v218 offset:53376
	ds_read_b64_tr_b16 v[160:161], v218 offset:54528
	ds_read_b128 v[128:131], v216 offset:36864
	ds_read_b64_tr_b16 v[162:163], v218 offset:53408
	ds_read_b64_tr_b16 v[164:165], v218 offset:54560
	s_waitcnt lgkmcnt(2)
	v_mfma_f32_16x16x32_bf16 v[64:67], v[158:161], v[128:131], v[64:67]
	ds_read_b64_tr_b16 v[166:167], v218 offset:53440
	ds_read_b64_tr_b16 v[168:169], v218 offset:54592
	s_waitcnt lgkmcnt(2)
	v_mfma_f32_16x16x32_bf16 v[60:63], v[162:165], v[128:131], v[60:63]
	ds_read_b64_tr_b16 v[170:171], v218 offset:53472
	ds_read_b64_tr_b16 v[172:173], v218 offset:54624
	s_waitcnt lgkmcnt(2)
	v_mfma_f32_16x16x32_bf16 v[56:59], v[166:169], v[128:131], v[56:59]
	ds_read_b128 v[132:135], v216 offset:37888
	s_waitcnt lgkmcnt(1)
	v_mfma_f32_16x16x32_bf16 v[52:55], v[170:173], v[128:131], v[52:55]
	ds_read_b128 v[136:139], v216 offset:38912
	s_waitcnt lgkmcnt(1)
	v_mfma_f32_16x16x32_bf16 v[48:51], v[158:161], v[132:135], v[48:51]
	ds_read_b128 v[140:143], v216 offset:39936
	v_mfma_f32_16x16x32_bf16 v[44:47], v[162:165], v[132:135], v[44:47]
	ds_read_b64_tr_b16 v[174:175], v218 offset:62592
	ds_read_b64_tr_b16 v[176:177], v218 offset:63744
	v_mfma_f32_16x16x32_bf16 v[40:43], v[166:169], v[132:135], v[40:43]
	ds_read_b64_tr_b16 v[178:179], v218 offset:62624
	ds_read_b64_tr_b16 v[180:181], v218 offset:63776
	v_mfma_f32_16x16x32_bf16 v[36:39], v[170:173], v[132:135], v[36:39]
	ds_read_b128 v[128:131], v216 offset:45120
	s_waitcnt lgkmcnt(6)
	v_mfma_f32_16x16x32_bf16 v[28:31], v[158:161], v[136:139], v[28:31]
	ds_read_b64_tr_b16 v[182:183], v218 offset:62656
	ds_read_b64_tr_b16 v[184:185], v218 offset:63808
	v_mfma_f32_16x16x32_bf16 v[24:27], v[162:165], v[136:139], v[24:27]
	ds_read_b64_tr_b16 v[186:187], v218 offset:62688
	ds_read_b64_tr_b16 v[188:189], v218 offset:63840
	v_mfma_f32_16x16x32_bf16 v[16:19], v[166:169], v[136:139], v[16:19]
	s_waitcnt vmcnt(8)
	ds_write_b128 v215, v[80:83]
	v_mfma_f32_16x16x32_bf16 v[12:15], v[170:173], v[136:139], v[12:15]
	ds_read_b128 v[132:135], v216 offset:46144
	s_waitcnt lgkmcnt(11)
	v_mfma_f32_16x16x32_bf16 v[8:11], v[158:161], v[140:143], v[8:11]
	ds_write_b128 v215, v[68:71] offset:2048
	v_mfma_f32_16x16x32_bf16 v[4:7], v[162:165], v[140:143], v[4:7]
	ds_write_b128 v215, v[72:75] offset:4096
	v_mfma_f32_16x16x32_bf16 v[32:35], v[166:169], v[140:143], v[32:35]
	ds_write_b128 v215, v[76:79] offset:6144
	v_mfma_f32_16x16x32_bf16 v[20:23], v[170:173], v[140:143], v[20:23]
	ds_read_b128 v[136:139], v216 offset:47168
	s_waitcnt lgkmcnt(10)
	v_mfma_f32_16x16x32_bf16 v[64:67], v[174:177], v[128:131], v[64:67]
	ds_write_b128 v217, v[88:91] offset:16512
	v_mfma_f32_16x16x32_bf16 v[60:63], v[178:181], v[128:131], v[60:63]
	ds_write_b128 v217, v[96:99] offset:21120
	s_waitcnt lgkmcnt(10)
	v_mfma_f32_16x16x32_bf16 v[56:59], v[182:185], v[128:131], v[56:59]
	ds_write_b128 v217, v[108:111] offset:25728
	s_waitcnt lgkmcnt(9)
	v_mfma_f32_16x16x32_bf16 v[52:55], v[186:189], v[128:131], v[52:55]
	ds_read_b128 v[140:143], v216 offset:48192
	s_waitcnt lgkmcnt(8)
	v_mfma_f32_16x16x32_bf16 v[48:51], v[174:177], v[132:135], v[48:51]
	ds_write_b128 v217, v[112:115] offset:30336
	v_mfma_f32_16x16x32_bf16 v[44:47], v[178:181], v[132:135], v[44:47]
	global_load_dwordx4 v[80:83], v206, s[44:45] offset:512
	v_mfma_f32_16x16x32_bf16 v[40:43], v[182:185], v[132:135], v[40:43]
	global_load_dwordx4 v[68:71], v207, s[44:45] offset:512
	v_mfma_f32_16x16x32_bf16 v[36:39], v[186:189], v[132:135], v[36:39]
	global_load_dwordx4 v[72:75], v208, s[44:45] offset:512
	s_waitcnt lgkmcnt(5)
	v_mfma_f32_16x16x32_bf16 v[28:31], v[174:177], v[136:139], v[28:31]
	global_load_dwordx4 v[76:79], v209, s[44:45] offset:512
	v_mfma_f32_16x16x32_bf16 v[24:27], v[178:181], v[136:139], v[24:27]
	global_load_dwordx4 v[88:91], v210, s[100:101]
	v_mfma_f32_16x16x32_bf16 v[16:19], v[182:185], v[136:139], v[16:19]
	global_load_dwordx4 v[96:99], v211, s[100:101]
	v_mfma_f32_16x16x32_bf16 v[12:15], v[186:189], v[136:139], v[12:15]
	global_load_dwordx4 v[108:111], v212, s[100:101]
	s_waitcnt lgkmcnt(1)
	v_mfma_f32_16x16x32_bf16 v[8:11], v[174:177], v[140:143], v[8:11]
	global_load_dwordx4 v[112:115], v213, s[100:101]
	v_mfma_f32_16x16x32_bf16 v[4:7], v[178:181], v[140:143], v[4:7]
	v_mfma_f32_16x16x32_bf16 v[32:35], v[182:185], v[140:143], v[32:35]
	v_mfma_f32_16x16x32_bf16 v[20:23], v[186:189], v[140:143], v[20:23]
	s_waitcnt lgkmcnt(0)
	s_barrier
	s_add_u32 s44, s44, 0x100
	s_addc_u32 s45, s45, 0
	s_add_u32 s46, s46, 0x90000
	s_addc_u32 s47, s47, 0
	s_add_u32 s100, s100, 0x90000
	s_addc_u32 s101, s101, 0
	s_add_i32 s6, s6, 2
	s_branch .Lip_loop
; #define LAS __attribute__((address_space(3)))
; __device__ __forceinline__ s16x4 lds_tr(lds_cptr p) { return __builtin_bit_cast(s16x4, __builtin_amdgcn_ds_read_tr16_b64_v4i16((LAS s16x4*)p)); }
;     ...
;     auto compute = [&]() __attribute__((always_inline)) {
; #pragma unroll
;         for (int kh = 0; kh < 2; ++kh) {
;             bf16x8 af[4], bfr[4];
; #pragma unroll
;             for (int m = 0; m < 4; ++m) af[m] = *(const LAS bf16x8*)(la + kh * GA_KH + m * 1024);
; #pragma unroll
;             for (int n = 0; n < 4; ++n) {
;                 const s16x4 r0 = lds_tr(lb + kh * 32 * GB_ST + n * 32), r1 = lds_tr(lb + kh * 32 * GB_ST + n * 32 + bsw);
;                 bfr[n] = (bf16x8){r0[0], r0[1], r0[2], r0[3], r1[0], r1[1], r1[2], r1[3]};
;             }
; #pragma unroll
;             for (int m = 0; m < 4; ++m)
; #pragma unroll
;                 for (int n = 0; n < 4; ++n) acc[m][n] = __builtin_amdgcn_mfma_f32_16x16x32_bf16(bfr[n], af[m], acc[m][n], 0, 0, 0);
;         }
;     };
;     ...
;     if (DEEP == 1) {
;         gloadA(0, ra0); gloadB(0, rb0); gloadA(1, ra1);
;         for (int kt = 0; kt < nk; kt += 2) {
;             __syncthreads();
;             lstore(ra0, rb0);
;             __syncthreads();
;             gloadB(kt + 1, rb0);
;             if (kt + 2 < nk) gloadA(kt + 2, ra0);
;             compute();
;             __syncthreads();
;             lstore(ra1, rb0);
;             __syncthreads();
;             if (kt + 2 < nk) gloadB(kt + 2, rb0);
;             if (kt + 3 < nk) gloadA(kt + 3, ra1);
;             compute();
;         }
;         return;
;     }
.Lip_h1_last:
	ds_read_b64_tr_b16 v[158:159], v218 offset:53376
	ds_read_b64_tr_b16 v[160:161], v218 offset:54528
	ds_read_b128 v[128:131], v216 offset:36864
	ds_read_b64_tr_b16 v[162:163], v218 offset:53408
	ds_read_b64_tr_b16 v[164:165], v218 offset:54560
	s_waitcnt lgkmcnt(2)
	v_mfma_f32_16x16x32_bf16 v[64:67], v[158:161], v[128:131], v[64:67]
	ds_read_b64_tr_b16 v[166:167], v218 offset:53440
	ds_read_b64_tr_b16 v[168:169], v218 offset:54592
	s_waitcnt lgkmcnt(2)
	v_mfma_f32_16x16x32_bf16 v[60:63], v[162:165], v[128:131], v[60:63]
	ds_read_b64_tr_b16 v[170:171], v218 offset:53472
	ds_read_b64_tr_b16 v[172:173], v218 offset:54624
	s_waitcnt lgkmcnt(2)
	v_mfma_f32_16x16x32_bf16 v[56:59], v[166:169], v[128:131], v[56:59]
	ds_read_b128 v[132:135], v216 offset:37888
	s_waitcnt lgkmcnt(1)
	v_mfma_f32_16x16x32_bf16 v[52:55], v[170:173], v[128:131], v[52:55]
	ds_read_b128 v[136:139], v216 offset:38912
	s_waitcnt lgkmcnt(1)
	v_mfma_f32_16x16x32_bf16 v[48:51], v[158:161], v[132:135], v[48:51]
	ds_read_b128 v[140:143], v216 offset:39936
	v_mfma_f32_16x16x32_bf16 v[44:47], v[162:165], v[132:135], v[44:47]
	ds_read_b64_tr_b16 v[174:175], v218 offset:62592
	ds_read_b64_tr_b16 v[176:177], v218 offset:63744
	v_mfma_f32_16x16x32_bf16 v[40:43], v[166:169], v[132:135], v[40:43]
	ds_read_b64_tr_b16 v[178:179], v218 offset:62624
	ds_read_b64_tr_b16 v[180:181], v218 offset:63776
	v_mfma_f32_16x16x32_bf16 v[36:39], v[170:173], v[132:135], v[36:39]
	ds_read_b128 v[128:131], v216 offset:45120
	s_waitcnt lgkmcnt(6)
	v_mfma_f32_16x16x32_bf16 v[28:31], v[158:161], v[136:139], v[28:31]
	ds_read_b64_tr_b16 v[182:183], v218 offset:62656
	ds_read_b64_tr_b16 v[184:185], v218 offset:63808
	v_mfma_f32_16x16x32_bf16 v[24:27], v[162:165], v[136:139], v[24:27]
	ds_read_b64_tr_b16 v[186:187], v218 offset:62688
	ds_read_b64_tr_b16 v[188:189], v218 offset:63840
	v_mfma_f32_16x16x32_bf16 v[16:19], v[166:169], v[136:139], v[16:19]
	s_waitcnt vmcnt(8)
	ds_write_b128 v215, v[80:83]
	v_mfma_f32_16x16x32_bf16 v[12:15], v[170:173], v[136:139], v[12:15]
	ds_read_b128 v[132:135], v216 offset:46144
	s_waitcnt lgkmcnt(11)
	v_mfma_f32_16x16x32_bf16 v[8:11], v[158:161], v[140:143], v[8:11]
	ds_write_b128 v215, v[68:71] offset:2048
	v_mfma_f32_16x16x32_bf16 v[4:7], v[162:165], v[140:143], v[4:7]
	ds_write_b128 v215, v[72:75] offset:4096
	v_mfma_f32_16x16x32_bf16 v[32:35], v[166:169], v[140:143], v[32:35]
	ds_write_b128 v215, v[76:79] offset:6144
	v_mfma_f32_16x16x32_bf16 v[20:23], v[170:173], v[140:143], v[20:23]
	ds_read_b128 v[136:139], v216 offset:47168
	s_waitcnt lgkmcnt(10)
	v_mfma_f32_16x16x32_bf16 v[64:67], v[174:177], v[128:131], v[64:67]
	ds_write_b128 v217, v[88:91] offset:16512
	v_mfma_f32_16x16x32_bf16 v[60:63], v[178:181], v[128:131], v[60:63]
	ds_write_b128 v217, v[96:99] offset:21120
	s_waitcnt lgkmcnt(10)
	v_mfma_f32_16x16x32_bf16 v[56:59], v[182:185], v[128:131], v[56:59]
	ds_write_b128 v217, v[108:111] offset:25728
	s_waitcnt lgkmcnt(9)
	v_mfma_f32_16x16x32_bf16 v[52:55], v[186:189], v[128:131], v[52:55]
	ds_read_b128 v[140:143], v216 offset:48192
	s_waitcnt lgkmcnt(8)
	v_mfma_f32_16x16x32_bf16 v[48:51], v[174:177], v[132:135], v[48:51]
	ds_write_b128 v217, v[112:115] offset:30336
	v_mfma_f32_16x16x32_bf16 v[44:47], v[178:181], v[132:135], v[44:47]
	v_mfma_f32_16x16x32_bf16 v[40:43], v[182:185], v[132:135], v[40:43]
	v_mfma_f32_16x16x32_bf16 v[36:39], v[186:189], v[132:135], v[36:39]
	s_waitcnt lgkmcnt(5)
	v_mfma_f32_16x16x32_bf16 v[28:31], v[174:177], v[136:139], v[28:31]
	v_mfma_f32_16x16x32_bf16 v[24:27], v[178:181], v[136:139], v[24:27]
	v_mfma_f32_16x16x32_bf16 v[16:19], v[182:185], v[136:139], v[16:19]
	v_mfma_f32_16x16x32_bf16 v[12:15], v[186:189], v[136:139], v[12:15]
	s_waitcnt lgkmcnt(1)
	v_mfma_f32_16x16x32_bf16 v[8:11], v[174:177], v[140:143], v[8:11]
	v_mfma_f32_16x16x32_bf16 v[4:7], v[178:181], v[140:143], v[4:7]
	v_mfma_f32_16x16x32_bf16 v[32:35], v[182:185], v[140:143], v[32:35]
	v_mfma_f32_16x16x32_bf16 v[20:23], v[186:189], v[140:143], v[20:23]
	s_waitcnt lgkmcnt(0)
	s_barrier
	ds_read_b64_tr_b16 v[158:159], v218 offset:16512
	ds_read_b64_tr_b16 v[160:161], v218 offset:17664
	ds_read_b128 v[128:131], v216
	ds_read_b64_tr_b16 v[162:163], v218 offset:16544
	ds_read_b64_tr_b16 v[164:165], v218 offset:17696
	s_waitcnt lgkmcnt(2)
	v_mfma_f32_16x16x32_bf16 v[64:67], v[158:161], v[128:131], v[64:67]
	ds_read_b64_tr_b16 v[166:167], v218 offset:16576
	ds_read_b64_tr_b16 v[168:169], v218 offset:17728
	s_waitcnt lgkmcnt(2)
	v_mfma_f32_16x16x32_bf16 v[60:63], v[162:165], v[128:131], v[60:63]
	ds_read_b64_tr_b16 v[170:171], v218 offset:16608
	ds_read_b64_tr_b16 v[172:173], v218 offset:17760
	s_waitcnt lgkmcnt(2)
	v_mfma_f32_16x16x32_bf16 v[56:59], v[166:169], v[128:131], v[56:59]
	ds_read_b128 v[132:135], v216 offset:1024
	s_waitcnt lgkmcnt(1)
	v_mfma_f32_16x16x32_bf16 v[52:55], v[170:173], v[128:131], v[52:55]
	ds_read_b128 v[136:139], v216 offset:2048
	s_waitcnt lgkmcnt(1)
	v_mfma_f32_16x16x32_bf16 v[48:51], v[158:161], v[132:135], v[48:51]
	ds_read_b128 v[140:143], v216 offset:3072
	v_mfma_f32_16x16x32_bf16 v[44:47], v[162:165], v[132:135], v[44:47]
	ds_read_b64_tr_b16 v[174:175], v218 offset:25728
	ds_read_b64_tr_b16 v[176:177], v218 offset:26880
	v_mfma_f32_16x16x32_bf16 v[40:43], v[166:169], v[132:135], v[40:43]
	ds_read_b64_tr_b16 v[178:179], v218 offset:25760
	ds_read_b64_tr_b16 v[180:181], v218 offset:26912
	v_mfma_f32_16x16x32_bf16 v[36:39], v[170:173], v[132:135], v[36:39]
	ds_read_b128 v[128:131], v216 offset:8256
	s_waitcnt lgkmcnt(6)
; #define LAS __attribute__((address_space(3)))
; __device__ __forceinline__ s16x4 lds_tr(lds_cptr p) { return __builtin_bit_cast(s16x4, __builtin_amdgcn_ds_read_tr16_b64_v4i16((LAS s16x4*)p)); }
;     ...
;     auto compute = [&]() __attribute__((always_inline)) {
; #pragma unroll
;         for (int kh = 0; kh < 2; ++kh) {
;             bf16x8 af[4], bfr[4];
; #pragma unroll
;             for (int m = 0; m < 4; ++m) af[m] = *(const LAS bf16x8*)(la + kh * GA_KH + m * 1024);
; #pragma unroll
;             for (int n = 0; n < 4; ++n) {
;                 const s16x4 r0 = lds_tr(lb + kh * 32 * GB_ST + n * 32), r1 = lds_tr(lb + kh * 32 * GB_ST + n * 32 + bsw);
;                 bfr[n] = (bf16x8){r0[0], r0[1], r0[2], r0[3], r1[0], r1[1], r1[2], r1[3]};
;             }
; #pragma unroll
;             for (int m = 0; m < 4; ++m)
; #pragma unroll
;                 for (int n = 0; n < 4; ++n) acc[m][n] = __builtin_amdgcn_mfma_f32_16x16x32_bf16(bfr[n], af[m], acc[m][n], 0, 0, 0);
;         }
;     };
;     ...
;     if (DEEP == 1) {
;         gloadA(0, ra0); gloadB(0, rb0); gloadA(1, ra1);
;         for (int kt = 0; kt < nk; kt += 2) {
;             __syncthreads();
;             lstore(ra0, rb0);
;             __syncthreads();
;             gloadB(kt + 1, rb0);
;             if (kt + 2 < nk) gloadA(kt + 2, ra0);
;             compute();
;             __syncthreads();
;             lstore(ra1, rb0);
;             __syncthreads();
;             if (kt + 2 < nk) gloadB(kt + 2, rb0);
;             if (kt + 3 < nk) gloadA(kt + 3, ra1);
;             compute();
;         }
;         return;
;     }
	v_mfma_f32_16x16x32_bf16 v[28:31], v[158:161], v[136:139], v[28:31]
	ds_read_b64_tr_b16 v[182:183], v218 offset:25792
	ds_read_b64_tr_b16 v[184:185], v218 offset:26944
	v_mfma_f32_16x16x32_bf16 v[24:27], v[162:165], v[136:139], v[24:27]
	ds_read_b64_tr_b16 v[186:187], v218 offset:25824
	ds_read_b64_tr_b16 v[188:189], v218 offset:26976
	v_mfma_f32_16x16x32_bf16 v[16:19], v[166:169], v[136:139], v[16:19]
	s_waitcnt vmcnt(0)
	ds_write_b128 v215, v[84:87] offset:36864
	v_mfma_f32_16x16x32_bf16 v[12:15], v[170:173], v[136:139], v[12:15]
	ds_read_b128 v[132:135], v216 offset:9280
	s_waitcnt lgkmcnt(11)
	v_mfma_f32_16x16x32_bf16 v[8:11], v[158:161], v[140:143], v[8:11]
	ds_write_b128 v215, v[92:95] offset:38912
	v_mfma_f32_16x16x32_bf16 v[4:7], v[162:165], v[140:143], v[4:7]
	ds_write_b128 v215, v[100:103] offset:40960
	v_mfma_f32_16x16x32_bf16 v[32:35], v[166:169], v[140:143], v[32:35]
	ds_write_b128 v215, v[104:107] offset:43008
	v_mfma_f32_16x16x32_bf16 v[20:23], v[170:173], v[140:143], v[20:23]
	ds_read_b128 v[136:139], v216 offset:10304
	s_waitcnt lgkmcnt(10)
	v_mfma_f32_16x16x32_bf16 v[64:67], v[174:177], v[128:131], v[64:67]
	ds_write_b128 v214, v[190:193] offset:16512
	v_mfma_f32_16x16x32_bf16 v[60:63], v[178:181], v[128:131], v[60:63]
	ds_write_b128 v214, v[194:197] offset:21120
	s_waitcnt lgkmcnt(10)
	v_mfma_f32_16x16x32_bf16 v[56:59], v[182:185], v[128:131], v[56:59]
	ds_write_b128 v214, v[198:201] offset:25728
	s_waitcnt lgkmcnt(9)
	v_mfma_f32_16x16x32_bf16 v[52:55], v[186:189], v[128:131], v[52:55]
	ds_read_b128 v[140:143], v216 offset:11328
	s_waitcnt lgkmcnt(8)
	v_mfma_f32_16x16x32_bf16 v[48:51], v[174:177], v[132:135], v[48:51]
	ds_write_b128 v214, v[202:205] offset:30336
	v_mfma_f32_16x16x32_bf16 v[44:47], v[178:181], v[132:135], v[44:47]
	v_mfma_f32_16x16x32_bf16 v[40:43], v[182:185], v[132:135], v[40:43]
	v_mfma_f32_16x16x32_bf16 v[36:39], v[186:189], v[132:135], v[36:39]
	s_waitcnt lgkmcnt(5)
	v_mfma_f32_16x16x32_bf16 v[28:31], v[174:177], v[136:139], v[28:31]
	v_mfma_f32_16x16x32_bf16 v[24:27], v[178:181], v[136:139], v[24:27]
	v_mfma_f32_16x16x32_bf16 v[16:19], v[182:185], v[136:139], v[16:19]
	v_mfma_f32_16x16x32_bf16 v[12:15], v[186:189], v[136:139], v[12:15]
	s_waitcnt lgkmcnt(1)
	v_mfma_f32_16x16x32_bf16 v[8:11], v[174:177], v[140:143], v[8:11]
	v_mfma_f32_16x16x32_bf16 v[4:7], v[178:181], v[140:143], v[4:7]
	v_mfma_f32_16x16x32_bf16 v[32:35], v[182:185], v[140:143], v[32:35]
	v_mfma_f32_16x16x32_bf16 v[20:23], v[186:189], v[140:143], v[20:23]
	s_waitcnt lgkmcnt(0)
	s_barrier
	ds_read_b64_tr_b16 v[158:159], v218 offset:53376
	ds_read_b64_tr_b16 v[160:161], v218 offset:54528
	ds_read_b128 v[128:131], v216 offset:36864
	ds_read_b64_tr_b16 v[162:163], v218 offset:53408
	ds_read_b64_tr_b16 v[164:165], v218 offset:54560
	s_waitcnt lgkmcnt(2)
	v_mfma_f32_16x16x32_bf16 v[64:67], v[158:161], v[128:131], v[64:67]
	ds_read_b64_tr_b16 v[166:167], v218 offset:53440
	ds_read_b64_tr_b16 v[168:169], v218 offset:54592
	s_waitcnt lgkmcnt(2)
	v_mfma_f32_16x16x32_bf16 v[60:63], v[162:165], v[128:131], v[60:63]
	ds_read_b64_tr_b16 v[170:171], v218 offset:53472
	ds_read_b64_tr_b16 v[172:173], v218 offset:54624
	s_waitcnt lgkmcnt(2)
	v_mfma_f32_16x16x32_bf16 v[56:59], v[166:169], v[128:131], v[56:59]
	ds_read_b128 v[132:135], v216 offset:37888
	s_waitcnt lgkmcnt(1)
	v_mfma_f32_16x16x32_bf16 v[52:55], v[170:173], v[128:131], v[52:55]
	ds_read_b128 v[136:139], v216 offset:38912
	s_waitcnt lgkmcnt(1)
	v_mfma_f32_16x16x32_bf16 v[48:51], v[158:161], v[132:135], v[48:51]
	ds_read_b128 v[140:143], v216 offset:39936
	v_mfma_f32_16x16x32_bf16 v[44:47], v[162:165], v[132:135], v[44:47]
	ds_read_b64_tr_b16 v[174:175], v218 offset:62592
	ds_read_b64_tr_b16 v[176:177], v218 offset:63744
	v_mfma_f32_16x16x32_bf16 v[40:43], v[166:169], v[132:135], v[40:43]
	ds_read_b64_tr_b16 v[178:179], v218 offset:62624
	ds_read_b64_tr_b16 v[180:181], v218 offset:63776
	v_mfma_f32_16x16x32_bf16 v[36:39], v[170:173], v[132:135], v[36:39]
	ds_read_b128 v[128:131], v216 offset:45120
	s_waitcnt lgkmcnt(6)
	v_mfma_f32_16x16x32_bf16 v[28:31], v[158:161], v[136:139], v[28:31]
	ds_read_b64_tr_b16 v[182:183], v218 offset:62656
	ds_read_b64_tr_b16 v[184:185], v218 offset:63808
	v_mfma_f32_16x16x32_bf16 v[24:27], v[162:165], v[136:139], v[24:27]
	ds_read_b64_tr_b16 v[186:187], v218 offset:62688
	ds_read_b64_tr_b16 v[188:189], v218 offset:63840
	v_mfma_f32_16x16x32_bf16 v[16:19], v[166:169], v[136:139], v[16:19]
	v_mfma_f32_16x16x32_bf16 v[12:15], v[170:173], v[136:139], v[12:15]
	ds_read_b128 v[132:135], v216 offset:46144
	s_waitcnt lgkmcnt(10)
	v_mfma_f32_16x16x32_bf16 v[8:11], v[158:161], v[140:143], v[8:11]
	v_mfma_f32_16x16x32_bf16 v[4:7], v[162:165], v[140:143], v[4:7]
	v_mfma_f32_16x16x32_bf16 v[32:35], v[166:169], v[140:143], v[32:35]
	v_mfma_f32_16x16x32_bf16 v[20:23], v[170:173], v[140:143], v[20:23]
	ds_read_b128 v[136:139], v216 offset:47168
	s_waitcnt lgkmcnt(6)
	v_mfma_f32_16x16x32_bf16 v[64:67], v[174:177], v[128:131], v[64:67]
	v_mfma_f32_16x16x32_bf16 v[60:63], v[178:181], v[128:131], v[60:63]
	s_waitcnt lgkmcnt(4)
	v_mfma_f32_16x16x32_bf16 v[56:59], v[182:185], v[128:131], v[56:59]
	s_waitcnt lgkmcnt(2)
	v_mfma_f32_16x16x32_bf16 v[52:55], v[186:189], v[128:131], v[52:55]
	ds_read_b128 v[140:143], v216 offset:48192
	s_waitcnt lgkmcnt(2)
	v_mfma_f32_16x16x32_bf16 v[48:51], v[174:177], v[132:135], v[48:51]
	v_mfma_f32_16x16x32_bf16 v[44:47], v[178:181], v[132:135], v[44:47]
	v_mfma_f32_16x16x32_bf16 v[40:43], v[182:185], v[132:135], v[40:43]
	v_mfma_f32_16x16x32_bf16 v[36:39], v[186:189], v[132:135], v[36:39]
	s_waitcnt lgkmcnt(1)
	v_mfma_f32_16x16x32_bf16 v[28:31], v[174:177], v[136:139], v[28:31]
	v_mfma_f32_16x16x32_bf16 v[24:27], v[178:181], v[136:139], v[24:27]
	v_mfma_f32_16x16x32_bf16 v[16:19], v[182:185], v[136:139], v[16:19]
	v_mfma_f32_16x16x32_bf16 v[12:15], v[186:189], v[136:139], v[12:15]
	s_waitcnt lgkmcnt(0)
	v_mfma_f32_16x16x32_bf16 v[8:11], v[174:177], v[140:143], v[8:11]
	v_mfma_f32_16x16x32_bf16 v[4:7], v[178:181], v[140:143], v[4:7]
	v_mfma_f32_16x16x32_bf16 v[32:35], v[182:185], v[140:143], v[32:35]
	v_mfma_f32_16x16x32_bf16 v[20:23], v[186:189], v[140:143], v[20:23]
	s_waitcnt lgkmcnt(0)
	s_barrier

; #define CAS __attribute__((address_space(4)))
; __global__ void __launch_bounds__(NTHR, 2) mk_fwd(Params prm) {
;     __shared__ __attribute__((aligned(16))) unsigned char smem_raw[S3_LDS_END];
;     float* smem = (float*)(smem_raw + GEMM_LDS);
;     Ctx c; c.p = (const CAS Params*)__builtin_amdgcn_kernarg_segment_ptr(); c.smf = smem; c.tid = threadIdx.x;
	.amdhsa_kernel _ZN12_GLOBAL__N_16mk_fwdENS_6ParamsE
		.amdhsa_group_segment_fixed_size 72704
		.amdhsa_private_segment_fixed_size 0
		.amdhsa_kernarg_size 576
		.amdhsa_user_sgpr_count 2
		.amdhsa_user_sgpr_dispatch_ptr 0
		.amdhsa_user_sgpr_queue_ptr 0
		.amdhsa_user_sgpr_kernarg_segment_ptr 1
		.amdhsa_user_sgpr_dispatch_id 0
		.amdhsa_user_sgpr_kernarg_preload_length 0
		.amdhsa_user_sgpr_kernarg_preload_offset 0
		.amdhsa_user_sgpr_private_segment_size 0
		.amdhsa_uses_dynamic_stack 0
		.amdhsa_enable_private_segment 0
		.amdhsa_system_sgpr_workgroup_id_x 1
		.amdhsa_system_sgpr_workgroup_id_y 0
		.amdhsa_system_sgpr_workgroup_id_z 0
		.amdhsa_system_sgpr_workgroup_info 0
		.amdhsa_system_vgpr_workitem_id 0
		.amdhsa_next_free_vgpr 254
		.amdhsa_next_free_sgpr 102
		.amdhsa_accum_offset 256
		.amdhsa_reserve_vcc 1
		.amdhsa_float_round_mode_32 0
		.amdhsa_float_round_mode_16_64 0
		.amdhsa_float_denorm_mode_32 3
		.amdhsa_float_denorm_mode_16_64 3
		.amdhsa_dx10_clamp 1
		.amdhsa_ieee_mode 1
		.amdhsa_fp16_overflow 0
		.amdhsa_tg_split 0
		.amdhsa_exception_fp_ieee_invalid_op 0
		.amdhsa_exception_fp_denorm_src 0
		.amdhsa_exception_fp_ieee_div_zero 0
		.amdhsa_exception_fp_ieee_overflow 0
		.amdhsa_exception_fp_ieee_underflow 0
		.amdhsa_exception_fp_ieee_inexact 0
		.amdhsa_exception_int_div_zero 0
	.end_amdhsa_kernel

; #define CAS __attribute__((address_space(4)))
; __global__ void __launch_bounds__(NTHR, 2) mk_fwd(Params prm) {
;     __shared__ __attribute__((aligned(16))) unsigned char smem_raw[S3_LDS_END];
;     float* smem = (float*)(smem_raw + GEMM_LDS);
;     Ctx c; c.p = (const CAS Params*)__builtin_amdgcn_kernarg_segment_ptr(); c.smf = smem; c.tid = threadIdx.x;
amdhsa.kernels:
  - .agpr_count:     0
    .args:
      - .offset:         0
        .size:           320
        .value_kind:     by_value
      - .offset:         320
        .size:           4
        .value_kind:     hidden_block_count_x
      - .offset:         324
        .size:           4
        .value_kind:     hidden_block_count_y
      - .offset:         328
        .size:           4
        .value_kind:     hidden_block_count_z
      - .offset:         332
        .size:           2
        .value_kind:     hidden_group_size_x
      - .offset:         334
        .size:           2
        .value_kind:     hidden_group_size_y
      - .offset:         336
        .size:           2
        .value_kind:     hidden_group_size_z
      - .offset:         338
        .size:           2
        .value_kind:     hidden_remainder_x
      - .offset:         340
        .size:           2
        .value_kind:     hidden_remainder_y
      - .offset:         342
        .size:           2
        .value_kind:     hidden_remainder_z
      - .offset:         360
        .size:           8
        .value_kind:     hidden_global_offset_x
      - .offset:         368
        .size:           8
        .value_kind:     hidden_global_offset_y
      - .offset:         376
        .size:           8
        .value_kind:     hidden_global_offset_z
      - .offset:         384
        .size:           2
        .value_kind:     hidden_grid_dims
    .group_segment_fixed_size: 72704
    .kernarg_segment_align: 8
    .kernarg_segment_size: 576
    .language:       OpenCL C
    .language_version:
      - 2
      - 0
    .max_flat_workgroup_size: 256
    .name:           _ZN12_GLOBAL__N_16mk_fwdENS_6ParamsE
    .private_segment_fixed_size: 0
    .sgpr_count:     108
    .sgpr_spill_count: 144
    .symbol:         _ZN12_GLOBAL__N_16mk_fwdENS_6ParamsE.kd
    .uniform_work_group_size: 1
    .uses_dynamic_stack: false
    .vgpr_count:     254
    .vgpr_spill_count: 0
    .wavefront_size: 64
